# baseline (speedup 1.0000x reference)
.LBB2_22:
	ds_read_b128 v[170:173], v174
	ds_read_b128 v[180:183], v174 offset:2048
	ds_read_b128 v[202:205], v178
	ds_read_b128 v[206:209], v178 offset:2048
	s_mov_b32 s89, s65
	s_mov_b32 s65, s6
	ds_read_b128 v[162:165], v194
	ds_read_b128 v[150:153], v194 offset:2048
	ds_read_b128 v[166:169], v195
	ds_read_b128 v[154:157], v195 offset:2048
	ds_read_b128 v[146:149], v194 offset:4096
	ds_read_b128 v[138:141], v194 offset:6144
	ds_read_b128 v[158:161], v195 offset:4096
	ds_read_b128 v[142:145], v195 offset:6144
	s_waitcnt vmcnt(14)
	s_mul_i32 s94, s83, s35
	v_cvt_pk_f16_f32 v22, v22, v23
	v_cvt_pk_f16_f32 v23, v24, v25
	v_cvt_pk_f16_f32 v18, v18, v19
	v_cvt_pk_f16_f32 v19, v20, v21
	v_cvt_pk_f16_f32 v14, v14, v15
	v_cvt_pk_f16_f32 v15, v16, v17
	v_cvt_pk_f16_f32 v10, v10, v11
	v_cvt_pk_f16_f32 v11, v12, v13
	ds_write2st64_b64 v201, v[22:23], v[18:19] offset0:32 offset1:40
	ds_write2st64_b64 v201, v[14:15], v[10:11] offset0:48 offset1:56
	s_waitcnt vmcnt(12)
	s_lshl_b32 s6, s90, 6
	s_add_i32 s7, s94, s6
	s_lshl_b32 s7, s7, 2
	v_add_u32_e32 v210, s89, v193
	s_add_i32 s8, s7, s81
	s_mul_i32 s95, s84, s35
	ds_write_b128 v210, v[6:9] offset:32768
	ds_write_b128 v210, v[2:5] offset:40960
	s_add_i32 s9, s8, s81
	s_add_i32 s93, s95, s6
	s_add_i32 s10, s9, s81
	s_nop 4
	buffer_load_dwordx4 v[22:25], v192, s[56:59], s7 offen nt
	buffer_load_dwordx4 v[18:21], v192, s[56:59], s8 offen nt
	buffer_load_dwordx4 v[14:17], v192, s[56:59], s9 offen nt
	buffer_load_dwordx4 v[10:13], v192, s[56:59], s10 offen nt
	s_lshl_b32 s6, s93, 1
	s_add_i32 s7, s6, s81
	s_nop 4
	buffer_load_dwordx4 v[6:9], v191, s[48:51], s6 offen
	buffer_load_dwordx4 v[2:5], v191, s[48:51], s7 offen
	s_barrier
	s_waitcnt lgkmcnt(0)
	s_setprio 1
	s_waitcnt lgkmcnt(11)
	v_mfma_f32_16x16x32_f16 v[134:137], v[170:173], v[162:165], v[134:137]
	v_mfma_f32_16x16x32_f16 v[130:133], v[180:183], v[162:165], v[130:133]
	s_waitcnt lgkmcnt(10)
	v_mfma_f32_16x16x32_f16 v[126:129], v[170:173], v[150:153], v[126:129]
	v_mfma_f32_16x16x32_f16 v[122:125], v[180:183], v[150:153], v[122:125]
	s_waitcnt lgkmcnt(7)
	v_mfma_f32_16x16x32_f16 v[118:121], v[170:173], v[146:149], v[118:121]
	v_mfma_f32_16x16x32_f16 v[114:117], v[180:183], v[146:149], v[114:117]
	s_waitcnt lgkmcnt(6)
	v_mfma_f32_16x16x32_f16 v[110:113], v[170:173], v[138:141], v[110:113]
	v_mfma_f32_16x16x32_f16 v[106:109], v[180:183], v[138:141], v[106:109]
	v_mfma_f32_16x16x32_f16 v[134:137], v[202:205], v[166:169], v[134:137]
	v_mfma_f32_16x16x32_f16 v[130:133], v[206:209], v[166:169], v[130:133]
	v_mfma_f32_16x16x32_f16 v[126:129], v[202:205], v[154:157], v[126:129]
	v_mfma_f32_16x16x32_f16 v[122:125], v[206:209], v[154:157], v[122:125]
	s_waitcnt lgkmcnt(5)
	v_mfma_f32_16x16x32_f16 v[118:121], v[202:205], v[158:161], v[118:121]
	v_mfma_f32_16x16x32_f16 v[114:117], v[206:209], v[158:161], v[114:117]
	s_waitcnt lgkmcnt(4)
	v_mfma_f32_16x16x32_f16 v[110:113], v[202:205], v[142:145], v[110:113]
	v_mfma_f32_16x16x32_f16 v[106:109], v[206:209], v[142:145], v[106:109]
	s_setprio 0
	s_barrier
	ds_read_b128 v[170:173], v174 offset:16384
	ds_read_b128 v[174:177], v174 offset:18432
	ds_read_b128 v[182:185], v178 offset:16384
	ds_read_b128 v[178:181], v178 offset:18432
	s_waitcnt vmcnt(16)
	s_cmp_lt_u32 s92, 32
	ds_write_b128 v210, v[30:33] offset:49152
	ds_write_b128 v210, v[26:29] offset:57344
	s_waitcnt vmcnt(15)
	s_cbranch_scc0 .LBB2_28
	s_add_i32 s38, s64, s92
	s_lshl_b64 s[60:61], s[38:39], 3
	s_add_u32 s60, s60, s85
	v_cmp_ne_u32_e64 s[6:7], 0, v34
	v_cmp_ne_u32_e64 s[8:9], 0, v35
	v_cmp_ne_u32_e64 s[10:11], 0, v36
	v_cmp_ne_u32_e64 s[12:13], 0, v37
	s_addc_u32 s61, s61, 0
	s_nop 1
	s_and_b64 s[98:99], s[6:7], s[8:9]
	s_and_b64 s[100:101], s[10:11], s[12:13]
	s_and_b64 s[98:99], s[98:99], s[100:101]
	s_cmp_eq_u64 s[98:99], -1
	s_cbranch_scc0 .Lqkv_mslow_0
	s_lshl_b64 s[96:97], s[60:61], 5
	v_lshl_add_u64 v[26:27], v[0:1], 0, s[96:97]
	v_mov_b32_e32 v28, -1
	v_mov_b32_e32 v29, -1
	s_add_u32 s6, s42, s60
	s_addc_u32 s7, s43, s61
	s_mov_b64 exec, 15
	global_store_dwordx2 v[26:27], v[28:29], off
	s_mov_b64 exec, 1
	global_store_byte v187, v187, s[6:7]
	s_mov_b64 exec, -1
.LBB2_28:
	s_add_i32 s93, s93, s81
	s_lshl_b32 s6, s93, 1
	s_add_i32 s91, s92, 2
	s_add_i32 s7, s6, s81
	s_add_i32 s8, s47, 0xffffe000
	s_cmp_lt_u32 s91, 32
	buffer_load_dwordx4 v[30:33], v191, s[48:51], s6 offen
	buffer_load_dwordx4 v[26:29], v191, s[48:51], s7 offen
	s_cselect_b64 s[6:7], -1, 0
	v_cndmask_b32_e64 v202, v200, v190, s[6:7]
	s_and_b64 s[6:7], s[6:7], exec
	s_cselect_b32 s6, s8, 0
	buffer_load_dwordx4 v[34:37], v202, s[52:55], s6 offen nt
	s_add_i32 s90, s90, 1
	s_cmp_lg_u32 s90, s82
	s_cbranch_scc1 .LBB2_32
	s_add_i32 s93, s86, 1
	s_cmp_gt_i32 s86, 1
	s_cbranch_scc1 .LBB2_31
	s_mul_i32 s6, s93, s33
	s_add_i32 s6, s6, s73
	s_abs_i32 s8, s6
	s_mul_hi_u32 s9, s8, s75
	s_mul_i32 s10, s9, s72
	s_ashr_i32 s7, s6, 31
	s_sub_i32 s8, s8, s10
	s_xor_b32 s7, s7, s74
	s_add_i32 s10, s9, 1
	s_sub_i32 s11, s8, s72
	s_cmp_ge_u32 s8, s72
	s_cselect_b32 s9, s10, s9
	s_cselect_b32 s8, s11, s8
	s_add_i32 s10, s9, 1
	s_cmp_ge_u32 s8, s72
	s_cselect_b32 s8, s10, s9
	s_xor_b32 s8, s8, s7
	s_sub_i32 s7, s8, s7
	s_mul_i32 s8, s7, s71
	s_sub_i32 s6, s6, s8
	s_abs_i32 s9, s6
	s_mul_hi_u32 s10, s9, s78
	s_mul_i32 s11, s10, s76
	s_ashr_i32 s8, s6, 31
	s_sub_i32 s9, s9, s11
	s_xor_b32 s8, s8, s77
	s_add_i32 s11, s10, 1
	s_sub_i32 s12, s9, s76
	s_cmp_ge_u32 s9, s76
	s_cselect_b32 s10, s11, s10
	s_cselect_b32 s9, s12, s9
	s_add_i32 s11, s10, 1
	s_cmp_ge_u32 s9, s76
	s_cselect_b32 s9, s11, s10
	s_xor_b32 s9, s9, s8
	s_sub_i32 s8, s9, s8
	s_lshl_b32 s83, s8, 7
	s_mul_i32 s8, s8, s70
	s_sub_i32 s6, s6, s8
	s_lshl_b32 s84, s6, 8
	s_cmp_eq_u32 s7, 1
	s_cselect_b32 s6, s19, s21
	s_cselect_b32 s8, s18, s20
	s_cselect_b32 s9, s25, s27
	s_cselect_b32 s10, s24, s26
	s_cmp_eq_u32 s7, 0
	s_cselect_b32 s6, s17, s6
	s_cselect_b32 s7, s23, s9
	s_cselect_b32 s56, s16, s8
	s_cselect_b32 s48, s22, s10
	s_and_b32 s57, s6, 0xffff
	s_and_b32 s49, s7, 0xffff
	s_mov_b32 s51, s15
	s_mul_i32 s94, s83, s35
	s_mul_i32 s95, s84, s35
	s_mov_b64 s[58:59], s[14:15]

.LBB2_33:
	s_barrier
	s_waitcnt lgkmcnt(0)
	s_setprio 1
	s_waitcnt lgkmcnt(5)
	v_mfma_f32_16x16x32_f16 v[102:105], v[170:173], v[162:165], v[102:105]
	s_waitcnt lgkmcnt(4)
	v_mfma_f32_16x16x32_f16 v[98:101], v[174:177], v[162:165], v[98:101]
	v_mfma_f32_16x16x32_f16 v[94:97], v[170:173], v[150:153], v[94:97]
	v_mfma_f32_16x16x32_f16 v[90:93], v[174:177], v[150:153], v[90:93]
	v_mfma_f32_16x16x32_f16 v[86:89], v[170:173], v[146:149], v[86:89]
	v_mfma_f32_16x16x32_f16 v[82:85], v[174:177], v[146:149], v[82:85]
	v_mfma_f32_16x16x32_f16 v[78:81], v[170:173], v[138:141], v[78:81]
	v_mfma_f32_16x16x32_f16 v[74:77], v[174:177], v[138:141], v[74:77]
	s_waitcnt lgkmcnt(3)
	v_mfma_f32_16x16x32_f16 v[102:105], v[182:185], v[166:169], v[102:105]
	s_waitcnt lgkmcnt(2)
	v_mfma_f32_16x16x32_f16 v[98:101], v[178:181], v[166:169], v[98:101]
	v_mfma_f32_16x16x32_f16 v[94:97], v[182:185], v[154:157], v[94:97]
	v_mfma_f32_16x16x32_f16 v[90:93], v[178:181], v[154:157], v[90:93]
	v_mfma_f32_16x16x32_f16 v[86:89], v[182:185], v[158:161], v[86:89]
	v_mfma_f32_16x16x32_f16 v[82:85], v[178:181], v[158:161], v[82:85]
	v_mfma_f32_16x16x32_f16 v[78:81], v[182:185], v[142:145], v[78:81]
	v_mfma_f32_16x16x32_f16 v[74:77], v[178:181], v[142:145], v[74:77]
	s_setprio 0
	s_barrier
	v_add_u32_e32 v202, s89, v196
	v_add_u32_e32 v203, s89, v186
	ds_read_b128 v[170:173], v202 offset:32768
	ds_read_b128 v[174:177], v202 offset:34816
	ds_read_b128 v[178:181], v203 offset:32768
	ds_read_b128 v[182:185], v203 offset:34816
	ds_read_b128 v[162:165], v194 offset:16384
	ds_read_b128 v[150:153], v194 offset:18432
	ds_read_b128 v[166:169], v195 offset:16384
	ds_read_b128 v[154:157], v195 offset:18432
	ds_read_b128 v[146:149], v194 offset:20480
	ds_read_b128 v[138:141], v194 offset:22528
	ds_read_b128 v[158:161], v195 offset:20480
	ds_read_b128 v[142:145], v195 offset:22528
	s_waitcnt vmcnt(14)
	s_lshl_b32 s86, s90, 6
	v_cvt_pk_f16_f32 v58, v58, v59
	v_cvt_pk_f16_f32 v59, v60, v61
	v_cvt_pk_f16_f32 v54, v54, v55
	v_cvt_pk_f16_f32 v55, v56, v57
	v_cvt_pk_f16_f32 v50, v50, v51
	v_cvt_pk_f16_f32 v51, v52, v53
	v_cvt_pk_f16_f32 v46, v46, v47
	v_cvt_pk_f16_f32 v47, v48, v49
	ds_write2st64_b64 v201, v[58:59], v[54:55] offset1:8
	ds_write2st64_b64 v201, v[50:51], v[46:47] offset0:16 offset1:24
	s_waitcnt vmcnt(12)
	s_add_i32 s6, s94, s86
	s_lshl_b32 s6, s6, 2
	v_add_u32_e32 v204, s87, v193
	s_add_i32 s7, s6, s81
	ds_write_b128 v204, v[42:45] offset:32768
	ds_write_b128 v204, v[38:41] offset:40960
	s_add_i32 s8, s7, s81
	s_add_i32 s9, s8, s81
	s_nop 4
	buffer_load_dwordx4 v[58:61], v192, s[56:59], s6 offen nt
	buffer_load_dwordx4 v[54:57], v192, s[56:59], s7 offen nt
	buffer_load_dwordx4 v[50:53], v192, s[56:59], s8 offen nt
	buffer_load_dwordx4 v[46:49], v192, s[56:59], s9 offen nt
	s_add_i32 s6, s95, s86
	s_lshl_b32 s6, s6, 1
	s_add_i32 s7, s6, s81
	s_nop 4
	buffer_load_dwordx4 v[42:45], v191, s[48:51], s6 offen
	buffer_load_dwordx4 v[38:41], v191, s[48:51], s7 offen
	s_barrier
	s_waitcnt lgkmcnt(0)
	s_setprio 1
	s_waitcnt lgkmcnt(11)
	v_mfma_f32_16x16x32_f16 v[134:137], v[170:173], v[162:165], v[134:137]
	v_mfma_f32_16x16x32_f16 v[130:133], v[174:177], v[162:165], v[130:133]
	s_waitcnt lgkmcnt(10)
	v_mfma_f32_16x16x32_f16 v[126:129], v[170:173], v[150:153], v[126:129]
	v_mfma_f32_16x16x32_f16 v[122:125], v[174:177], v[150:153], v[122:125]
	s_waitcnt lgkmcnt(7)
	v_mfma_f32_16x16x32_f16 v[118:121], v[170:173], v[146:149], v[118:121]
	v_mfma_f32_16x16x32_f16 v[114:117], v[174:177], v[146:149], v[114:117]
	s_waitcnt lgkmcnt(6)
	v_mfma_f32_16x16x32_f16 v[110:113], v[170:173], v[138:141], v[110:113]
	v_mfma_f32_16x16x32_f16 v[106:109], v[174:177], v[138:141], v[106:109]
	v_mfma_f32_16x16x32_f16 v[134:137], v[178:181], v[166:169], v[134:137]
	v_mfma_f32_16x16x32_f16 v[130:133], v[182:185], v[166:169], v[130:133]
	v_mfma_f32_16x16x32_f16 v[126:129], v[178:181], v[154:157], v[126:129]
	v_mfma_f32_16x16x32_f16 v[122:125], v[182:185], v[154:157], v[122:125]
	s_waitcnt lgkmcnt(5)
	v_mfma_f32_16x16x32_f16 v[118:121], v[178:181], v[158:161], v[118:121]
	v_mfma_f32_16x16x32_f16 v[114:117], v[182:185], v[158:161], v[114:117]
	s_waitcnt lgkmcnt(4)
	v_mfma_f32_16x16x32_f16 v[110:113], v[178:181], v[142:145], v[110:113]
	v_mfma_f32_16x16x32_f16 v[106:109], v[182:185], v[142:145], v[106:109]
	s_setprio 0
	s_barrier
	ds_read_b128 v[170:173], v202 offset:49152
	ds_read_b128 v[174:177], v202 offset:51200
	ds_read_b128 v[182:185], v203 offset:49152
	ds_read_b128 v[178:181], v203 offset:51200
	s_waitcnt vmcnt(16)
	s_cmp_gt_u32 s92, 30
	ds_write_b128 v204, v[66:69] offset:49152
	ds_write_b128 v204, v[62:65] offset:57344
	s_waitcnt vmcnt(15)
	s_cbranch_scc1 .LBB2_39
	s_add_i32 s38, s64, s92
	s_add_i32 s38, s38, 1
	s_lshl_b64 s[60:61], s[38:39], 3
	s_add_u32 s60, s60, s85
	v_cmp_ne_u32_e64 s[6:7], 0, v70
	v_cmp_ne_u32_e64 s[8:9], 0, v71
	v_cmp_ne_u32_e64 s[10:11], 0, v72
	v_cmp_ne_u32_e64 s[12:13], 0, v73
	s_addc_u32 s61, s61, 0
	s_nop 1
	s_and_b64 s[98:99], s[6:7], s[8:9]
	s_and_b64 s[100:101], s[10:11], s[12:13]
	s_and_b64 s[98:99], s[98:99], s[100:101]
	s_cmp_eq_u64 s[98:99], -1
	s_cbranch_scc0 .Lqkv_mslow_1
	s_lshl_b64 s[94:95], s[60:61], 5
	v_lshl_add_u64 v[62:63], v[0:1], 0, s[94:95]
	v_mov_b32_e32 v64, -1
	v_mov_b32_e32 v65, -1
	s_add_u32 s6, s42, s60
	s_addc_u32 s7, s43, s61
	s_mov_b64 exec, 15
	global_store_dwordx2 v[62:63], v[64:65], off
	s_mov_b64 exec, 1
	global_store_byte v187, v187, s[6:7]
	s_mov_b64 exec, -1
.LBB2_39:
	s_add_i32 s6, s84, 0x80
	s_mul_i32 s6, s6, s35
	s_add_i32 s6, s6, s86
	s_lshl_b32 s6, s6, 1
	s_add_i32 s7, s6, s81
	s_cmp_lt_u32 s91, 31
	buffer_load_dwordx4 v[66:69], v191, s[48:51], s6 offen
	buffer_load_dwordx4 v[62:65], v191, s[48:51], s7 offen
	s_cselect_b64 s[6:7], -1, 0
	v_cndmask_b32_e64 v202, v200, v190, s[6:7]
	s_and_b64 s[6:7], s[6:7], exec
	s_cselect_b32 s6, s47, 0
	buffer_load_dwordx4 v[70:73], v202, s[52:55], s6 offen nt
	s_add_i32 s90, s90, 1
	s_cmp_lg_u32 s90, s82
	s_cbranch_scc1 .LBB2_43
	s_add_i32 s86, s93, 1
	s_cmp_gt_i32 s93, 1
	s_cbranch_scc1 .LBB2_42
	s_mul_i32 s6, s86, s33
	s_add_i32 s6, s6, s73
	s_abs_i32 s8, s6
	s_mul_hi_u32 s9, s8, s75
	s_mul_i32 s10, s9, s72
	s_ashr_i32 s7, s6, 31
	s_sub_i32 s8, s8, s10
	s_xor_b32 s7, s7, s74
	s_add_i32 s10, s9, 1
	s_sub_i32 s11, s8, s72
	s_cmp_ge_u32 s8, s72
	s_cselect_b32 s9, s10, s9
	s_cselect_b32 s8, s11, s8
	s_add_i32 s10, s9, 1
	s_cmp_ge_u32 s8, s72
	s_cselect_b32 s8, s10, s9
	s_xor_b32 s8, s8, s7
	s_sub_i32 s7, s8, s7
	s_mul_i32 s8, s7, s71
	s_sub_i32 s6, s6, s8
	s_abs_i32 s9, s6
	s_mul_hi_u32 s10, s9, s78
	s_mul_i32 s11, s10, s76
	s_ashr_i32 s8, s6, 31
	s_sub_i32 s9, s9, s11
	s_xor_b32 s8, s8, s77
	s_add_i32 s11, s10, 1
	s_sub_i32 s12, s9, s76
	s_cmp_ge_u32 s9, s76
	s_cselect_b32 s10, s11, s10
	s_cselect_b32 s9, s12, s9
	s_add_i32 s11, s10, 1
	s_cmp_ge_u32 s9, s76
	s_cselect_b32 s9, s11, s10
	s_xor_b32 s9, s9, s8
	s_sub_i32 s8, s9, s8
	s_lshl_b32 s83, s8, 7
	s_mul_i32 s8, s8, s70
	s_sub_i32 s6, s6, s8
	s_lshl_b32 s84, s6, 8
	s_cmp_eq_u32 s7, 1
	s_cselect_b32 s6, s19, s21
	s_cselect_b32 s8, s18, s20
	s_cselect_b32 s9, s25, s27
	s_cselect_b32 s10, s24, s26
	s_cmp_eq_u32 s7, 0
	s_cselect_b32 s6, s17, s6
	s_cselect_b32 s7, s23, s9
	s_cselect_b32 s56, s16, s8
	s_cselect_b32 s48, s22, s10
	s_and_b32 s57, s6, 0xffff
	s_and_b32 s49, s7, 0xffff
	s_mov_b32 s51, s15
	s_mov_b64 s[58:59], s[14:15]

.LBB2_44:
	s_barrier
	s_waitcnt lgkmcnt(0)
	s_setprio 1
	s_waitcnt lgkmcnt(5)
	v_mfma_f32_16x16x32_f16 v[102:105], v[170:173], v[162:165], v[102:105]
	s_waitcnt lgkmcnt(4)
	v_mfma_f32_16x16x32_f16 v[98:101], v[174:177], v[162:165], v[98:101]
	v_mfma_f32_16x16x32_f16 v[94:97], v[170:173], v[150:153], v[94:97]
	v_mfma_f32_16x16x32_f16 v[90:93], v[174:177], v[150:153], v[90:93]
	v_mfma_f32_16x16x32_f16 v[86:89], v[170:173], v[146:149], v[86:89]
	v_mfma_f32_16x16x32_f16 v[82:85], v[174:177], v[146:149], v[82:85]
	v_mfma_f32_16x16x32_f16 v[78:81], v[170:173], v[138:141], v[78:81]
	v_mfma_f32_16x16x32_f16 v[74:77], v[174:177], v[138:141], v[74:77]
	s_waitcnt lgkmcnt(3)
	v_mfma_f32_16x16x32_f16 v[102:105], v[182:185], v[166:169], v[102:105]
	s_waitcnt lgkmcnt(2)
	v_mfma_f32_16x16x32_f16 v[98:101], v[178:181], v[166:169], v[98:101]
	v_mfma_f32_16x16x32_f16 v[94:97], v[182:185], v[154:157], v[94:97]
	v_mfma_f32_16x16x32_f16 v[90:93], v[178:181], v[154:157], v[90:93]
	v_mfma_f32_16x16x32_f16 v[86:89], v[182:185], v[158:161], v[86:89]
	v_mfma_f32_16x16x32_f16 v[82:85], v[178:181], v[158:161], v[82:85]
	v_mfma_f32_16x16x32_f16 v[78:81], v[182:185], v[142:145], v[78:81]
	v_mfma_f32_16x16x32_f16 v[74:77], v[178:181], v[142:145], v[74:77]
	s_setprio 0
	s_barrier
	s_add_i32 s6, s63, 2
	s_cmp_lg_u32 s6, s82
	s_cbranch_scc1 .LBB2_21
	s_mul_i32 s6, s88, s33
	s_add_i32 s6, s6, s73
	s_abs_i32 s8, s6
	s_mul_hi_u32 s9, s8, s75
	s_mul_i32 s10, s9, s72
	s_ashr_i32 s7, s6, 31
	s_sub_i32 s8, s8, s10
	s_xor_b32 s7, s7, s74
	s_add_i32 s10, s9, 1
	s_sub_i32 s11, s8, s72
	s_cmp_ge_u32 s8, s72
	s_cselect_b32 s9, s10, s9
	s_cselect_b32 s8, s11, s8
	s_add_i32 s10, s9, 1
	s_cmp_ge_u32 s8, s72
	s_cselect_b32 s8, s10, s9
	s_xor_b32 s8, s8, s7
	s_sub_i32 s8, s8, s7
	s_mul_i32 s7, s8, s71
	s_sub_i32 s6, s6, s7
	s_abs_i32 s9, s6
	s_mul_hi_u32 s10, s9, s78
	s_mul_i32 s11, s10, s76
	s_ashr_i32 s7, s6, 31
	s_sub_i32 s9, s9, s11
	s_xor_b32 s7, s7, s77
	s_add_i32 s11, s10, 1
	s_sub_i32 s12, s9, s76
	s_cmp_ge_u32 s9, s76
	s_cselect_b32 s10, s11, s10
	s_cselect_b32 s9, s12, s9
	s_add_i32 s11, s10, 1
	s_cmp_ge_u32 s9, s76
	s_cselect_b32 s9, s11, s10
	s_xor_b32 s9, s9, s7
	s_sub_i32 s10, s9, s7
	s_mul_i32 s7, s10, s70
	s_sub_i32 s11, s6, s7
	s_cmp_eq_u32 s8, 0
	s_cselect_b64 s[6:7], -1, 0
	s_cmp_eq_u32 s8, 1
	v_mov_b32_e32 v139, s46
	v_mov_b32_e32 v140, s45
	s_cselect_b64 s[8:9], -1, 0
	v_mov_b32_e32 v138, s44
	v_cndmask_b32_e64 v139, v139, v140, s[8:9]
	s_and_b64 s[8:9], s[8:9], exec
	v_cndmask_b32_e64 v138, v139, v138, s[6:7]
	s_cselect_b32 s8, s31, s37
	s_cselect_b32 s9, s30, s36
	s_and_b64 s[6:7], s[6:7], exec
	v_pk_mul_f32 v[134:135], v[138:139], v[134:135] op_sel_hi:[0,1]
	v_pk_mul_f32 v[136:137], v[138:139], v[136:137] op_sel_hi:[0,1]
	v_pk_mul_f32 v[130:131], v[138:139], v[130:131] op_sel_hi:[0,1]
	s_cselect_b32 s6, s29, s8
	s_mul_i32 s10, s10, s80
	v_cvt_pk_f16_f32 v134, v134, v135
	v_cvt_pk_f16_f32 v135, v136, v137
	v_cvt_pk_f16_f32 v136, v130, v131
	v_pk_mul_f32 v[130:131], v[138:139], v[132:133] op_sel_hi:[0,1]
	s_cselect_b32 s60, s28, s9
	s_and_b32 s61, s6, 0xffff
	s_lshl_b32 s6, s11, 9
	s_lshl_b32 s7, s10, 7
	v_cvt_pk_f16_f32 v137, v130, v131
	v_pk_mul_f32 v[126:127], v[138:139], v[126:127] op_sel_hi:[0,1]
	v_pk_mul_f32 v[128:129], v[138:139], v[128:129] op_sel_hi:[0,1]
	v_pk_mul_f32 v[122:123], v[138:139], v[122:123] op_sel_hi:[0,1]
	s_mov_b32 s63, s15
	s_add_i32 s8, s6, s7
	v_permlane16_swap_b32_e32 v134, v136
	v_permlane16_swap_b32_e32 v135, v137
	v_cvt_pk_f16_f32 v126, v126, v127
	v_cvt_pk_f16_f32 v127, v128, v129
	v_cvt_pk_f16_f32 v128, v122, v123
	v_pk_mul_f32 v[122:123], v[138:139], v[124:125] op_sel_hi:[0,1]
	buffer_store_dwordx4 v[134:137], v199, s[60:63], s8 offen
	s_add_i32 s8, s7, s34
	v_cvt_pk_f16_f32 v129, v122, v123
	v_pk_mul_f32 v[118:119], v[138:139], v[118:119] op_sel_hi:[0,1]
	v_pk_mul_f32 v[120:121], v[138:139], v[120:121] op_sel_hi:[0,1]
	v_pk_mul_f32 v[114:115], v[138:139], v[114:115] op_sel_hi:[0,1]
	s_add_i32 s9, s6, s8
	v_permlane16_swap_b32_e32 v126, v128
	v_permlane16_swap_b32_e32 v127, v129
	v_cvt_pk_f16_f32 v118, v118, v119
	v_cvt_pk_f16_f32 v119, v120, v121
	v_cvt_pk_f16_f32 v120, v114, v115
	v_pk_mul_f32 v[114:115], v[138:139], v[116:117] op_sel_hi:[0,1]
	buffer_store_dwordx4 v[126:129], v199, s[60:63], s9 offen
	s_add_i32 s9, s8, s34
	v_cvt_pk_f16_f32 v121, v114, v115
	s_add_i32 s10, s6, s9
	v_permlane16_swap_b32_e32 v118, v120
	v_permlane16_swap_b32_e32 v119, v121
	v_pk_mul_f32 v[110:111], v[138:139], v[110:111] op_sel_hi:[0,1]
	v_pk_mul_f32 v[112:113], v[138:139], v[112:113] op_sel_hi:[0,1]
	v_pk_mul_f32 v[106:107], v[138:139], v[106:107] op_sel_hi:[0,1]
	v_pk_mul_f32 v[102:103], v[138:139], v[102:103] op_sel_hi:[0,1]
	v_pk_mul_f32 v[104:105], v[138:139], v[104:105] op_sel_hi:[0,1]
	v_pk_mul_f32 v[98:99], v[138:139], v[98:99] op_sel_hi:[0,1]
	buffer_store_dwordx4 v[118:121], v199, s[60:63], s10 offen
	s_add_i32 s10, s9, s34
	v_cvt_pk_f16_f32 v110, v110, v111
	v_cvt_pk_f16_f32 v111, v112, v113
	v_cvt_pk_f16_f32 v112, v106, v107
	v_pk_mul_f32 v[106:107], v[138:139], v[108:109] op_sel_hi:[0,1]
	v_cvt_pk_f16_f32 v102, v102, v103
	v_cvt_pk_f16_f32 v103, v104, v105
	v_cvt_pk_f16_f32 v104, v98, v99
	v_pk_mul_f32 v[98:99], v[138:139], v[100:101] op_sel_hi:[0,1]
	v_pk_mul_f32 v[94:95], v[138:139], v[94:95] op_sel_hi:[0,1]
	v_pk_mul_f32 v[96:97], v[138:139], v[96:97] op_sel_hi:[0,1]
	v_pk_mul_f32 v[90:91], v[138:139], v[90:91] op_sel_hi:[0,1]
	s_add_i32 s11, s6, s10
	v_cvt_pk_f16_f32 v113, v106, v107
	s_bitset1_b32 s6, 8
	v_cvt_pk_f16_f32 v105, v98, v99
	v_cvt_pk_f16_f32 v94, v94, v95
	v_cvt_pk_f16_f32 v95, v96, v97
	v_cvt_pk_f16_f32 v96, v90, v91
	v_pk_mul_f32 v[90:91], v[138:139], v[92:93] op_sel_hi:[0,1]
	v_pk_mul_f32 v[86:87], v[138:139], v[86:87] op_sel_hi:[0,1]
	v_pk_mul_f32 v[88:89], v[138:139], v[88:89] op_sel_hi:[0,1]
	v_pk_mul_f32 v[82:83], v[138:139], v[82:83] op_sel_hi:[0,1]
	v_pk_mul_f32 v[78:79], v[138:139], v[78:79] op_sel_hi:[0,1]
	v_pk_mul_f32 v[80:81], v[138:139], v[80:81] op_sel_hi:[0,1]
	v_pk_mul_f32 v[74:75], v[138:139], v[74:75] op_sel_hi:[0,1]
	v_permlane16_swap_b32_e32 v110, v112
	v_permlane16_swap_b32_e32 v111, v113
	s_add_i32 s7, s6, s7
	v_permlane16_swap_b32_e32 v102, v104
	v_permlane16_swap_b32_e32 v103, v105
	v_cvt_pk_f16_f32 v97, v90, v91
	v_cvt_pk_f16_f32 v86, v86, v87
	v_cvt_pk_f16_f32 v87, v88, v89
	v_cvt_pk_f16_f32 v88, v82, v83
	v_pk_mul_f32 v[82:83], v[138:139], v[84:85] op_sel_hi:[0,1]
	v_cvt_pk_f16_f32 v78, v78, v79
	v_cvt_pk_f16_f32 v79, v80, v81
	v_cvt_pk_f16_f32 v80, v74, v75
	v_pk_mul_f32 v[74:75], v[138:139], v[76:77] op_sel_hi:[0,1]
	buffer_store_dwordx4 v[110:113], v199, s[60:63], s11 offen
	buffer_store_dwordx4 v[102:105], v199, s[60:63], s7 offen
	s_add_i32 s7, s6, s8
	v_permlane16_swap_b32_e32 v94, v96
	v_permlane16_swap_b32_e32 v95, v97
	v_cvt_pk_f16_f32 v89, v82, v83
	v_cvt_pk_f16_f32 v81, v74, v75
	buffer_store_dwordx4 v[94:97], v199, s[60:63], s7 offen
	s_add_i32 s7, s6, s9
	v_permlane16_swap_b32_e32 v86, v88
	v_permlane16_swap_b32_e32 v87, v89
	s_add_i32 s6, s6, s10
	v_permlane16_swap_b32_e32 v78, v80
	v_permlane16_swap_b32_e32 v79, v81
	v_mov_b32_e32 v74, 0
	buffer_store_dwordx4 v[86:89], v199, s[60:63], s7 offen
	buffer_store_dwordx4 v[78:81], v199, s[60:63], s6 offen
	s_add_i32 s88, s88, 1
	s_mov_b32 s63, -2
	v_mov_b32_e32 v75, v74
	v_mov_b32_e32 v76, v74
	v_mov_b32_e32 v77, v74
	v_mov_b32_e32 v78, v74
	v_mov_b32_e32 v79, v74
	v_mov_b32_e32 v80, v74
	v_mov_b32_e32 v81, v74
	v_mov_b32_e32 v82, v74
	v_mov_b32_e32 v83, v74
	v_mov_b32_e32 v84, v74
	v_mov_b32_e32 v85, v74
	v_mov_b32_e32 v86, v74
	v_mov_b32_e32 v87, v74
	v_mov_b32_e32 v88, v74
	v_mov_b32_e32 v89, v74
	v_mov_b32_e32 v90, v74
	v_mov_b32_e32 v91, v74
	v_mov_b32_e32 v92, v74
	v_mov_b32_e32 v93, v74
	v_mov_b32_e32 v94, v74
	v_mov_b32_e32 v95, v74
	v_mov_b32_e32 v96, v74
	v_mov_b32_e32 v97, v74
	v_mov_b32_e32 v98, v74
	v_mov_b32_e32 v99, v74
	v_mov_b32_e32 v100, v74
	v_mov_b32_e32 v101, v74
	v_mov_b32_e32 v102, v74
	v_mov_b32_e32 v103, v74
	v_mov_b32_e32 v104, v74
	v_mov_b32_e32 v105, v74
	v_mov_b32_e32 v106, v74
	v_mov_b32_e32 v107, v74
	v_mov_b32_e32 v108, v74
	v_mov_b32_e32 v109, v74
	v_mov_b32_e32 v110, v74
	v_mov_b32_e32 v111, v74
	v_mov_b32_e32 v112, v74
	v_mov_b32_e32 v113, v74
	v_mov_b32_e32 v114, v74
	v_mov_b32_e32 v115, v74
	v_mov_b32_e32 v116, v74
	v_mov_b32_e32 v117, v74
	v_mov_b32_e32 v118, v74
	v_mov_b32_e32 v119, v74
	v_mov_b32_e32 v120, v74
	v_mov_b32_e32 v121, v74
	v_mov_b32_e32 v122, v74
	v_mov_b32_e32 v123, v74
	v_mov_b32_e32 v124, v74
	v_mov_b32_e32 v125, v74
	v_mov_b32_e32 v126, v74
	v_mov_b32_e32 v127, v74
	v_mov_b32_e32 v128, v74
	v_mov_b32_e32 v129, v74
	v_mov_b32_e32 v130, v74
	v_mov_b32_e32 v131, v74
	v_mov_b32_e32 v132, v74
	v_mov_b32_e32 v133, v74
	v_mov_b32_e32 v134, v74
	v_mov_b32_e32 v135, v74
	v_mov_b32_e32 v136, v74
	v_mov_b32_e32 v137, v74
	s_branch .LBB2_21
.Lqkv_mslow_0:
	s_and_saveexec_b64 s[68:69], s[0:1]
	s_cbranch_execz .LBB2_25
	v_mov_b32_e32 v28, s13
	v_mov_b32_e32 v29, s11
	v_cndmask_b32_e64 v28, v28, v29, s[4:5]
	v_mov_b32_e32 v29, s12
	v_mov_b32_e32 v30, s10
	v_cndmask_b32_e64 v29, v29, v30, s[4:5]
	v_mov_b32_e32 v30, s8
	v_cndmask_b32_e64 v30, v29, v30, s[2:3]
	v_mov_b32_e32 v29, s9
	v_cndmask_b32_e64 v28, v28, v29, s[2:3]
	v_mov_b32_e32 v29, s7
	s_lshl_b64 s[96:97], s[60:61], 5
	v_cndmask_b32_e32 v29, v28, v29, vcc
	v_mov_b32_e32 v28, s6
	v_lshl_add_u64 v[26:27], v[0:1], 0, s[96:97]
	v_cndmask_b32_e32 v28, v30, v28, vcc
	global_store_dwordx2 v[26:27], v[28:29], off

.LBB2_27:
	s_or_b64 exec, exec, s[68:69]
	s_branch .LBB2_28
